# speedup vs baseline: 1.0032x; 1.0008x over previous
.LBB1_4:
	s_load_dwordx2 s[0:1], s[0:1], 0x0
	v_add_u32_e32 v2, 0xffffff00, v0
	v_ashrrev_i32_e32 v20, 4, v2
	v_add_u32_e32 v2, s12, v20
	v_ashrrev_i32_e32 v3, 31, v2
	v_lshlrev_b64 v[2:3], 12, v[2:3]
	s_lshl_b32 s2, s3, 6
	s_waitcnt lgkmcnt(0)
	v_lshl_add_u64 v[2:3], s[0:1], 0, v[2:3]
	v_lshlrev_b32_e32 v4, 4, v1
	v_mov_b32_e32 v5, 0
	s_and_b32 s6, s2, 0x3c0
	s_mov_b32 s1, 0
	v_lshl_add_u64 v[2:3], v[2:3], 0, v[4:5]
	s_lshl_b32 s0, s6, 2
	v_lshl_add_u64 v[16:17], v[2:3], 0, s[0:1]
	s_mov_b32 s3, 0x10000
	v_add_co_u32_e32 v12, vcc, s3, v16
	s_mov_b32 s4, 0x20000
	s_nop 0
	v_addc_co_u32_e32 v13, vcc, 0, v17, vcc
	global_load_dwordx4 v[4:7], v[16:17], off sc0 nt
	global_load_dwordx4 v[8:11], v[12:13], off sc0 nt
	v_add_co_u32_e32 v12, vcc, s4, v16
	s_mov_b32 s5, 0x30000
	s_nop 0
	v_addc_co_u32_e32 v13, vcc, 0, v17, vcc
	s_add_i32 s0, s2, 64
	global_load_dwordx4 v[12:15], v[12:13], off sc0 nt
	v_add_co_u32_e32 v16, vcc, s5, v16
	s_and_b32 s0, s0, 0x3c0
	s_nop 0
	v_addc_co_u32_e32 v17, vcc, 0, v17, vcc
	s_lshl_b32 s0, s0, 2
	global_load_dwordx4 v[16:19], v[16:17], off sc0 nt
	v_lshl_add_u64 v[28:29], v[2:3], 0, s[0:1]
	v_lshrrev_b32_e32 v1, 1, v1
	v_lshrrev_b32_e32 v21, 5, v0
	v_lshlrev_b32_e32 v0, 3, v0
	v_add_co_u32_e32 v30, vcc, s3, v28
	v_bitop3_b32 v1, v1, v21, 7 bitop3:0x78
	v_and_b32_e32 v0, 8, v0
	v_addc_co_u32_e32 v31, vcc, 0, v29, vcc
	v_lshl_or_b32 v0, v1, 4, v0
	v_add_co_u32_e32 v36, vcc, s4, v28
	v_lshl_or_b32 v0, v20, 7, v0
	global_load_dwordx4 v[20:23], v[28:29], off sc0 nt
	global_load_dwordx4 v[24:27], v[30:31], off sc0 nt
	v_addc_co_u32_e32 v37, vcc, 0, v29, vcc
	s_add_i32 s0, s2, 0x80
	v_add_co_u32_e32 v38, vcc, s5, v28
	s_and_b32 s0, s0, 0x3c0
	s_nop 0
	v_addc_co_u32_e32 v39, vcc, 0, v29, vcc
	global_load_dwordx4 v[28:31], v[36:37], off sc0 nt
	global_load_dwordx4 v[32:35], v[38:39], off sc0 nt
	s_lshl_b32 s0, s0, 2
	v_lshl_add_u64 v[44:45], v[2:3], 0, s[0:1]
	v_add_co_u32_e32 v46, vcc, s3, v44
	s_add_i32 s0, s2, 0xc0
	s_nop 0
	v_addc_co_u32_e32 v47, vcc, 0, v45, vcc
	v_add_co_u32_e32 v52, vcc, s4, v44
	global_load_dwordx4 v[36:39], v[44:45], off sc0 nt
	global_load_dwordx4 v[40:43], v[46:47], off sc0 nt
	v_addc_co_u32_e32 v53, vcc, 0, v45, vcc
	v_add_co_u32_e32 v54, vcc, s5, v44
	s_and_b32 s0, s0, 0x3c0
	s_nop 0
	v_addc_co_u32_e32 v55, vcc, 0, v45, vcc
	global_load_dwordx4 v[44:47], v[52:53], off sc0 nt
	global_load_dwordx4 v[48:51], v[54:55], off sc0 nt
	s_lshl_b32 s0, s0, 2
	v_lshl_add_u64 v[60:61], v[2:3], 0, s[0:1]
	v_add_co_u32_e32 v62, vcc, s3, v60
	s_add_i32 s0, s2, 0x100
	s_nop 0
	v_addc_co_u32_e32 v63, vcc, 0, v61, vcc
	v_add_co_u32_e32 v68, vcc, s4, v60
	global_load_dwordx4 v[52:55], v[60:61], off sc0 nt
	global_load_dwordx4 v[56:59], v[62:63], off sc0 nt
	v_addc_co_u32_e32 v69, vcc, 0, v61, vcc
	v_add_co_u32_e32 v70, vcc, s5, v60
	s_and_b32 s0, s0, 0x3c0
	s_nop 0
	v_addc_co_u32_e32 v71, vcc, 0, v61, vcc
	global_load_dwordx4 v[60:63], v[68:69], off sc0 nt
	global_load_dwordx4 v[64:67], v[70:71], off sc0 nt
	s_lshl_b32 s0, s0, 2
	v_add_u32_e32 v1, 0x10000, v0
	s_waitcnt vmcnt(15)
	v_cvt_pk_f16_f32 v7, v6, v7
	v_cvt_pk_f16_f32 v6, v4, v5
	s_waitcnt vmcnt(14)
	v_cvt_pk_f16_f32 v5, v10, v11
	v_cvt_pk_f16_f32 v4, v8, v9
	ds_write2st64_b64 v0, v[6:7], v[4:5] offset1:4
	s_waitcnt vmcnt(13)
	v_cvt_pk_f16_f32 v4, v12, v13
	v_lshl_add_u64 v[12:13], v[2:3], 0, s[0:1]
	v_cvt_pk_f16_f32 v5, v14, v15
	v_add_co_u32_e32 v14, vcc, s3, v12
	s_add_i32 s0, s2, 0x140
	s_nop 0
	v_addc_co_u32_e32 v15, vcc, 0, v13, vcc
	s_waitcnt vmcnt(12)
	v_cvt_pk_f16_f32 v7, v18, v19
	v_cvt_pk_f16_f32 v6, v16, v17
	ds_write2st64_b64 v0, v[4:5], v[6:7] offset0:8 offset1:12
	v_add_co_u32_e32 v68, vcc, s4, v12
	global_load_dwordx4 v[4:7], v[12:13], off sc0 nt
	global_load_dwordx4 v[8:11], v[14:15], off sc0 nt
	v_addc_co_u32_e32 v69, vcc, 0, v13, vcc
	v_add_co_u32_e32 v70, vcc, s5, v12
	s_and_b32 s0, s0, 0x3c0
	s_nop 0
	v_addc_co_u32_e32 v71, vcc, 0, v13, vcc
	global_load_dwordx4 v[12:15], v[68:69], off sc0 nt
	global_load_dwordx4 v[16:19], v[70:71], off sc0 nt
	s_waitcnt vmcnt(15)
	v_cvt_pk_f16_f32 v23, v22, v23
	v_cvt_pk_f16_f32 v22, v20, v21
	s_waitcnt vmcnt(14)
	v_cvt_pk_f16_f32 v21, v26, v27
	v_cvt_pk_f16_f32 v20, v24, v25
	s_lshl_b32 s0, s0, 2
	s_waitcnt lgkmcnt(0)
	v_add_u32_e32 v171, 1, v171
	ds_write_b32 v169, v171
	ds_write2st64_b64 v0, v[22:23], v[20:21] offset0:16 offset1:20
	s_waitcnt vmcnt(13)
	v_cvt_pk_f16_f32 v20, v28, v29
	v_lshl_add_u64 v[28:29], v[2:3], 0, s[0:1]
	v_cvt_pk_f16_f32 v21, v30, v31
	v_add_co_u32_e32 v30, vcc, s3, v28
	s_waitcnt vmcnt(12)
	v_cvt_pk_f16_f32 v23, v34, v35
	v_cvt_pk_f16_f32 v22, v32, v33
	v_addc_co_u32_e32 v31, vcc, 0, v29, vcc
	ds_write2st64_b64 v0, v[20:21], v[22:23] offset0:24 offset1:28
	v_add_co_u32_e32 v68, vcc, s4, v28
	global_load_dwordx4 v[20:23], v[28:29], off sc0 nt
	global_load_dwordx4 v[24:27], v[30:31], off sc0 nt
	v_addc_co_u32_e32 v69, vcc, 0, v29, vcc
	s_add_i32 s0, s2, 0x180
	v_add_co_u32_e32 v70, vcc, s5, v28
	s_and_b32 s0, s0, 0x3c0
	s_nop 0
	v_addc_co_u32_e32 v71, vcc, 0, v29, vcc
	global_load_dwordx4 v[28:31], v[68:69], off sc0 nt
	global_load_dwordx4 v[32:35], v[70:71], off sc0 nt
	s_waitcnt vmcnt(15)
	v_cvt_pk_f16_f32 v39, v38, v39
	v_cvt_pk_f16_f32 v38, v36, v37
	s_waitcnt vmcnt(14)
	v_cvt_pk_f16_f32 v37, v42, v43
	v_cvt_pk_f16_f32 v36, v40, v41
	s_lshl_b32 s0, s0, 2
	s_waitcnt lgkmcnt(0)
	v_add_u32_e32 v171, 1, v171
	ds_write_b32 v169, v171
	ds_write2st64_b64 v0, v[38:39], v[36:37] offset0:32 offset1:36
	s_waitcnt vmcnt(13)
	v_cvt_pk_f16_f32 v36, v44, v45
	v_lshl_add_u64 v[44:45], v[2:3], 0, s[0:1]
	v_cvt_pk_f16_f32 v37, v46, v47
	v_add_co_u32_e32 v46, vcc, s3, v44
	s_waitcnt vmcnt(12)
	v_cvt_pk_f16_f32 v39, v50, v51
	v_cvt_pk_f16_f32 v38, v48, v49
	v_addc_co_u32_e32 v47, vcc, 0, v45, vcc
	ds_write2st64_b64 v0, v[36:37], v[38:39] offset0:40 offset1:44
	v_add_co_u32_e32 v68, vcc, s4, v44
	global_load_dwordx4 v[36:39], v[44:45], off sc0 nt
	global_load_dwordx4 v[40:43], v[46:47], off sc0 nt
	v_addc_co_u32_e32 v69, vcc, 0, v45, vcc
	v_add_co_u32_e32 v70, vcc, s5, v44
	s_add_i32 s0, s2, 0x1c0
	s_nop 0
	v_addc_co_u32_e32 v71, vcc, 0, v45, vcc
	global_load_dwordx4 v[44:47], v[68:69], off sc0 nt
	global_load_dwordx4 v[48:51], v[70:71], off sc0 nt
	s_and_b32 s0, s0, 0x3c0
	s_waitcnt vmcnt(15)
	v_cvt_pk_f16_f32 v55, v54, v55
	v_cvt_pk_f16_f32 v54, v52, v53
	s_waitcnt vmcnt(14)
	v_cvt_pk_f16_f32 v53, v58, v59
	v_cvt_pk_f16_f32 v52, v56, v57
	s_lshl_b32 s0, s0, 2
	s_waitcnt lgkmcnt(0)
	v_add_u32_e32 v171, 1, v171
	ds_write_b32 v169, v171
	ds_write2st64_b64 v0, v[54:55], v[52:53] offset0:48 offset1:52
	s_waitcnt vmcnt(13)
	v_cvt_pk_f16_f32 v52, v60, v61
	v_lshl_add_u64 v[60:61], v[2:3], 0, s[0:1]
	v_cvt_pk_f16_f32 v53, v62, v63
	v_add_co_u32_e32 v62, vcc, s3, v60
	s_waitcnt vmcnt(12)
	v_cvt_pk_f16_f32 v55, v66, v67
	v_addc_co_u32_e32 v63, vcc, 0, v61, vcc
	v_cvt_pk_f16_f32 v54, v64, v65
	v_add_co_u32_e32 v68, vcc, s4, v60
	ds_write2st64_b64 v0, v[52:53], v[54:55] offset0:56 offset1:60
	s_nop 0
	v_addc_co_u32_e32 v69, vcc, 0, v61, vcc
	global_load_dwordx4 v[52:55], v[60:61], off sc0 nt
	global_load_dwordx4 v[56:59], v[62:63], off sc0 nt
	v_add_co_u32_e32 v70, vcc, s5, v60
	s_xor_b32 s0, s6, 0x200
	s_nop 0
	v_addc_co_u32_e32 v71, vcc, 0, v61, vcc
	global_load_dwordx4 v[60:63], v[68:69], off sc0 nt
	global_load_dwordx4 v[64:67], v[70:71], off sc0 nt
	s_waitcnt vmcnt(15)
	v_cvt_pk_f16_f32 v7, v6, v7
	v_cvt_pk_f16_f32 v6, v4, v5
	s_waitcnt vmcnt(14)
	v_cvt_pk_f16_f32 v5, v10, v11
	v_cvt_pk_f16_f32 v4, v8, v9
	s_lshl_b32 s0, s0, 2
	s_waitcnt lgkmcnt(0)
	v_add_u32_e32 v171, 1, v171
	ds_write_b32 v169, v171
	ds_write2st64_b64 v0, v[6:7], v[4:5] offset0:64 offset1:68
	s_waitcnt vmcnt(13)
	v_cvt_pk_f16_f32 v4, v12, v13
	v_lshl_add_u64 v[12:13], v[2:3], 0, s[0:1]
	v_cvt_pk_f16_f32 v5, v14, v15
	v_add_co_u32_e32 v14, vcc, s3, v12
	s_waitcnt vmcnt(12)
	v_cvt_pk_f16_f32 v7, v18, v19
	v_cvt_pk_f16_f32 v6, v16, v17
	v_addc_co_u32_e32 v15, vcc, 0, v13, vcc
	ds_write2st64_b64 v0, v[4:5], v[6:7] offset0:72 offset1:76
	v_add_co_u32_e32 v68, vcc, s4, v12
	global_load_dwordx4 v[4:7], v[12:13], off sc0 nt
	global_load_dwordx4 v[8:11], v[14:15], off sc0 nt
	v_addc_co_u32_e32 v69, vcc, 0, v13, vcc
	s_add_i32 s0, s2, 0x240
	v_add_co_u32_e32 v70, vcc, s5, v12
	s_and_b32 s0, s0, 0x3c0
	s_nop 0
	v_addc_co_u32_e32 v71, vcc, 0, v13, vcc
	global_load_dwordx4 v[12:15], v[68:69], off sc0 nt
	global_load_dwordx4 v[16:19], v[70:71], off sc0 nt
	s_waitcnt vmcnt(15)
	v_cvt_pk_f16_f32 v23, v22, v23
	v_cvt_pk_f16_f32 v22, v20, v21
	s_waitcnt vmcnt(14)
	v_cvt_pk_f16_f32 v21, v26, v27
	v_cvt_pk_f16_f32 v20, v24, v25
	s_lshl_b32 s0, s0, 2
	s_waitcnt lgkmcnt(0)
	v_add_u32_e32 v171, 1, v171
	ds_write_b32 v169, v171
	ds_write2st64_b64 v0, v[22:23], v[20:21] offset0:80 offset1:84
	s_waitcnt vmcnt(13)
	v_cvt_pk_f16_f32 v20, v28, v29
	v_lshl_add_u64 v[28:29], v[2:3], 0, s[0:1]
	v_cvt_pk_f16_f32 v21, v30, v31
	v_add_co_u32_e32 v30, vcc, s3, v28
	s_waitcnt vmcnt(12)
	v_cvt_pk_f16_f32 v23, v34, v35
	v_cvt_pk_f16_f32 v22, v32, v33
	v_addc_co_u32_e32 v31, vcc, 0, v29, vcc
	ds_write2st64_b64 v0, v[20:21], v[22:23] offset0:88 offset1:92
	v_add_co_u32_e32 v68, vcc, s4, v28
	global_load_dwordx4 v[20:23], v[28:29], off sc0 nt
	global_load_dwordx4 v[24:27], v[30:31], off sc0 nt
	v_addc_co_u32_e32 v69, vcc, 0, v29, vcc
	s_add_i32 s0, s2, 0x280
	v_add_co_u32_e32 v70, vcc, s5, v28
	s_and_b32 s0, s0, 0x3c0
	s_nop 0
	v_addc_co_u32_e32 v71, vcc, 0, v29, vcc
	global_load_dwordx4 v[28:31], v[68:69], off sc0 nt
	global_load_dwordx4 v[32:35], v[70:71], off sc0 nt
	s_waitcnt vmcnt(15)
	v_cvt_pk_f16_f32 v39, v38, v39
	v_cvt_pk_f16_f32 v38, v36, v37
	s_waitcnt vmcnt(14)
	v_cvt_pk_f16_f32 v37, v42, v43
	v_cvt_pk_f16_f32 v36, v40, v41
	s_lshl_b32 s0, s0, 2
	s_waitcnt lgkmcnt(0)
	v_add_u32_e32 v171, 1, v171
	ds_write_b32 v169, v171
	ds_write2st64_b64 v0, v[38:39], v[36:37] offset0:96 offset1:100
	s_waitcnt vmcnt(13)
	v_cvt_pk_f16_f32 v36, v44, v45
	v_lshl_add_u64 v[44:45], v[2:3], 0, s[0:1]
	v_cvt_pk_f16_f32 v37, v46, v47
	v_add_co_u32_e32 v46, vcc, s3, v44
	s_waitcnt vmcnt(12)
	v_cvt_pk_f16_f32 v39, v50, v51
	v_cvt_pk_f16_f32 v38, v48, v49
	v_addc_co_u32_e32 v47, vcc, 0, v45, vcc
	ds_write2st64_b64 v0, v[36:37], v[38:39] offset0:104 offset1:108
	v_add_co_u32_e32 v68, vcc, s4, v44
	global_load_dwordx4 v[36:39], v[44:45], off sc0 nt
	global_load_dwordx4 v[40:43], v[46:47], off sc0 nt
	v_addc_co_u32_e32 v69, vcc, 0, v45, vcc
	v_add_co_u32_e32 v70, vcc, s5, v44
	s_add_i32 s0, s2, 0x2c0
	s_nop 0
	v_addc_co_u32_e32 v71, vcc, 0, v45, vcc
	global_load_dwordx4 v[44:47], v[68:69], off sc0 nt
	global_load_dwordx4 v[48:51], v[70:71], off sc0 nt
	s_and_b32 s0, s0, 0x3c0
	s_waitcnt vmcnt(15)
	v_cvt_pk_f16_f32 v55, v54, v55
	v_cvt_pk_f16_f32 v54, v52, v53
	s_waitcnt vmcnt(14)
	v_cvt_pk_f16_f32 v53, v58, v59
	v_cvt_pk_f16_f32 v52, v56, v57
	s_lshl_b32 s0, s0, 2
	s_waitcnt lgkmcnt(0)
	v_add_u32_e32 v171, 1, v171
	ds_write_b32 v169, v171
	ds_write2st64_b64 v0, v[54:55], v[52:53] offset0:112 offset1:116
	s_waitcnt vmcnt(13)
	v_cvt_pk_f16_f32 v53, v62, v63
	v_cvt_pk_f16_f32 v52, v60, v61
	s_waitcnt vmcnt(12)
	v_cvt_pk_f16_f32 v55, v66, v67
	v_cvt_pk_f16_f32 v54, v64, v65
	v_lshl_add_u64 v[60:61], v[2:3], 0, s[0:1]
	ds_write2st64_b64 v0, v[52:53], v[54:55] offset0:120 offset1:124
	v_add_co_u32_e32 v62, vcc, s3, v60
	s_add_i32 s0, s2, 0x300
	s_nop 0
	v_addc_co_u32_e32 v63, vcc, 0, v61, vcc
	global_load_dwordx4 v[52:55], v[60:61], off sc0 nt
	global_load_dwordx4 v[56:59], v[62:63], off sc0 nt
	v_add_co_u32_e32 v68, vcc, s4, v60
	s_waitcnt vmcnt(13)
	v_cvt_pk_f16_f32 v7, v6, v7
	v_addc_co_u32_e32 v69, vcc, 0, v61, vcc
	v_add_co_u32_e32 v70, vcc, s5, v60
	v_cvt_pk_f16_f32 v6, v4, v5
	s_and_b32 s0, s0, 0x3c0
	v_addc_co_u32_e32 v71, vcc, 0, v61, vcc
	global_load_dwordx4 v[60:63], v[68:69], off sc0 nt
	global_load_dwordx4 v[64:67], v[70:71], off sc0 nt
	s_waitcnt lgkmcnt(0)
	v_add_u32_e32 v171, 1, v171
	ds_write_b32 v169, v171
	ds_write_b64 v1, v[6:7]
	s_waitcnt vmcnt(14)
	v_cvt_pk_f16_f32 v5, v10, v11
	v_cvt_pk_f16_f32 v4, v8, v9
	v_add_u32_e32 v1, 0x10800, v0
	s_lshl_b32 s0, s0, 2
	ds_write_b64 v1, v[4:5]
	s_waitcnt vmcnt(13)
	v_cvt_pk_f16_f32 v4, v12, v13
	v_lshl_add_u64 v[12:13], v[2:3], 0, s[0:1]
	v_cvt_pk_f16_f32 v5, v14, v15
	v_add_co_u32_e32 v14, vcc, s3, v12
	v_add_u32_e32 v1, 0x11000, v0
	s_nop 0
	v_addc_co_u32_e32 v15, vcc, 0, v13, vcc
	v_add_co_u32_e32 v68, vcc, s4, v12
	ds_write_b64 v1, v[4:5]
	s_waitcnt vmcnt(12)
	v_cvt_pk_f16_f32 v5, v18, v19
	v_cvt_pk_f16_f32 v4, v16, v17
	v_add_u32_e32 v1, 0x11800, v0
	v_addc_co_u32_e32 v69, vcc, 0, v13, vcc
	s_add_i32 s0, s2, 0x340
	ds_write_b64 v1, v[4:5]
	v_add_co_u32_e32 v70, vcc, s5, v12
	s_waitcnt vmcnt(11)
	v_cvt_pk_f16_f32 v23, v22, v23
	v_cvt_pk_f16_f32 v22, v20, v21
	v_add_u32_e32 v1, 0x12000, v0
	s_and_b32 s0, s0, 0x3c0
	global_load_dwordx4 v[4:7], v[12:13], off sc0 nt
	global_load_dwordx4 v[8:11], v[14:15], off sc0 nt
	v_addc_co_u32_e32 v71, vcc, 0, v13, vcc
	global_load_dwordx4 v[12:15], v[68:69], off sc0 nt
	global_load_dwordx4 v[16:19], v[70:71], off sc0 nt
	s_waitcnt lgkmcnt(0)
	v_add_u32_e32 v171, 1, v171
	ds_write_b32 v169, v171
	ds_write_b64 v1, v[22:23]
	s_waitcnt vmcnt(14)
	v_cvt_pk_f16_f32 v21, v26, v27
	v_cvt_pk_f16_f32 v20, v24, v25
	v_add_u32_e32 v1, 0x12800, v0
	s_lshl_b32 s0, s0, 2
	ds_write_b64 v1, v[20:21]
	s_waitcnt vmcnt(13)
	v_cvt_pk_f16_f32 v20, v28, v29
	v_lshl_add_u64 v[28:29], v[2:3], 0, s[0:1]
	v_cvt_pk_f16_f32 v21, v30, v31
	v_add_co_u32_e32 v30, vcc, s3, v28
	v_add_u32_e32 v1, 0x13000, v0
	s_nop 0
	v_addc_co_u32_e32 v31, vcc, 0, v29, vcc
	v_add_co_u32_e32 v68, vcc, s4, v28
	ds_write_b64 v1, v[20:21]
	s_waitcnt vmcnt(12)
	v_cvt_pk_f16_f32 v21, v34, v35
	v_cvt_pk_f16_f32 v20, v32, v33
	v_add_u32_e32 v1, 0x13800, v0
	v_addc_co_u32_e32 v69, vcc, 0, v29, vcc
	s_add_i32 s0, s2, 0x380
	ds_write_b64 v1, v[20:21]
	v_add_co_u32_e32 v70, vcc, s5, v28
	s_waitcnt vmcnt(11)
	v_cvt_pk_f16_f32 v39, v38, v39
	v_cvt_pk_f16_f32 v38, v36, v37
	v_add_u32_e32 v1, 0x14000, v0
	s_and_b32 s0, s0, 0x3c0
	global_load_dwordx4 v[20:23], v[28:29], off sc0 nt
	global_load_dwordx4 v[24:27], v[30:31], off sc0 nt
	v_addc_co_u32_e32 v71, vcc, 0, v29, vcc
	global_load_dwordx4 v[28:31], v[68:69], off sc0 nt
	global_load_dwordx4 v[32:35], v[70:71], off sc0 nt
	s_waitcnt lgkmcnt(0)
	v_add_u32_e32 v171, 1, v171
	ds_write_b32 v169, v171
	ds_write_b64 v1, v[38:39]
	s_waitcnt vmcnt(14)
	v_cvt_pk_f16_f32 v37, v42, v43
	v_cvt_pk_f16_f32 v36, v40, v41
	v_add_u32_e32 v1, 0x14800, v0
	s_lshl_b32 s0, s0, 2
	ds_write_b64 v1, v[36:37]
	s_waitcnt vmcnt(13)
	v_cvt_pk_f16_f32 v36, v44, v45
	v_lshl_add_u64 v[44:45], v[2:3], 0, s[0:1]
	v_cvt_pk_f16_f32 v37, v46, v47
	v_add_co_u32_e32 v46, vcc, s3, v44
	s_addk_i32 s2, 0x3c0
	s_nop 0
	v_addc_co_u32_e32 v47, vcc, 0, v45, vcc
	v_add_co_u32_e32 v68, vcc, s4, v44
	v_add_u32_e32 v1, 0x15000, v0
	s_nop 0
	v_addc_co_u32_e32 v69, vcc, 0, v45, vcc
	s_and_b32 s0, s2, 0x3c0
	ds_write_b64 v1, v[36:37]
	s_waitcnt vmcnt(12)
	v_cvt_pk_f16_f32 v37, v50, v51
	v_cvt_pk_f16_f32 v36, v48, v49
	v_add_u32_e32 v1, 0x15800, v0
	v_add_co_u32_e32 v70, vcc, s5, v44
	s_lshl_b32 s0, s0, 2
	ds_write_b64 v1, v[36:37]
	v_addc_co_u32_e32 v71, vcc, 0, v45, vcc
	v_lshl_add_u64 v[2:3], v[2:3], 0, s[0:1]
	global_load_dwordx4 v[36:39], v[44:45], off sc0 nt
	global_load_dwordx4 v[40:43], v[46:47], off sc0 nt
	s_waitcnt vmcnt(13)
	v_cvt_pk_f16_f32 v55, v54, v55
	v_cvt_pk_f16_f32 v54, v52, v53
	s_waitcnt vmcnt(12)
	v_cvt_pk_f16_f32 v52, v56, v57
	v_add_co_u32_e32 v56, vcc, s3, v2
	v_add_u32_e32 v1, 0x16000, v0
	s_nop 0
	v_addc_co_u32_e32 v57, vcc, 0, v3, vcc
	global_load_dwordx4 v[44:47], v[68:69], off sc0 nt
	global_load_dwordx4 v[48:51], v[70:71], off sc0 nt
	s_waitcnt lgkmcnt(0)
	v_add_u32_e32 v171, 1, v171
	ds_write_b32 v169, v171
	ds_write_b64 v1, v[54:55]
	v_cvt_pk_f16_f32 v53, v58, v59
	v_add_u32_e32 v1, 0x16800, v0
	v_add_co_u32_e32 v68, vcc, s4, v2
	ds_write_b64 v1, v[52:53]
	global_load_dwordx4 v[52:55], v[2:3], off sc0 nt
	v_addc_co_u32_e32 v69, vcc, 0, v3, vcc
	global_load_dwordx4 v[56:59], v[56:57], off sc0 nt
	v_add_co_u32_e32 v2, vcc, s5, v2
	global_load_dwordx4 v[68:71], v[68:69], off sc0 nt
	s_nop 0
	v_addc_co_u32_e32 v3, vcc, 0, v3, vcc
	global_load_dwordx4 v[72:75], v[2:3], off sc0 nt
	s_waitcnt vmcnt(17)
	v_cvt_pk_f16_f32 v63, v62, v63
	v_cvt_pk_f16_f32 v62, v60, v61
	v_add_u32_e32 v1, 0x17000, v0
	ds_write_b64 v1, v[62:63]
	s_waitcnt vmcnt(16)
	v_cvt_pk_f16_f32 v3, v66, v67
	v_cvt_pk_f16_f32 v2, v64, v65
	v_add_u32_e32 v1, 0x17800, v0
	ds_write_b64 v1, v[2:3]
	s_waitcnt vmcnt(15)
	v_cvt_pk_f16_f32 v3, v6, v7
	v_cvt_pk_f16_f32 v2, v4, v5
	v_add_u32_e32 v1, 0x18000, v0
	s_waitcnt lgkmcnt(0)
	v_add_u32_e32 v171, 1, v171
	ds_write_b32 v169, v171
	ds_write_b64 v1, v[2:3]
	s_waitcnt vmcnt(14)
	v_cvt_pk_f16_f32 v3, v10, v11
	v_cvt_pk_f16_f32 v2, v8, v9
	v_add_u32_e32 v1, 0x18800, v0
	ds_write_b64 v1, v[2:3]
	s_waitcnt vmcnt(13)
	v_cvt_pk_f16_f32 v3, v14, v15
	v_cvt_pk_f16_f32 v2, v12, v13
	v_add_u32_e32 v1, 0x19000, v0
	ds_write_b64 v1, v[2:3]
	s_waitcnt vmcnt(12)
	v_cvt_pk_f16_f32 v3, v18, v19
	v_cvt_pk_f16_f32 v2, v16, v17
	v_add_u32_e32 v1, 0x19800, v0
	ds_write_b64 v1, v[2:3]
	s_waitcnt vmcnt(11)
	v_cvt_pk_f16_f32 v3, v22, v23
	v_cvt_pk_f16_f32 v2, v20, v21
	v_add_u32_e32 v1, 0x1a000, v0
	s_waitcnt lgkmcnt(0)
	v_add_u32_e32 v171, 1, v171
	ds_write_b32 v169, v171
	ds_write_b64 v1, v[2:3]
	s_waitcnt vmcnt(10)
	v_cvt_pk_f16_f32 v3, v26, v27
	v_cvt_pk_f16_f32 v2, v24, v25
	v_add_u32_e32 v1, 0x1a800, v0
	ds_write_b64 v1, v[2:3]
	s_waitcnt vmcnt(9)
	v_cvt_pk_f16_f32 v3, v30, v31
	v_cvt_pk_f16_f32 v2, v28, v29
	v_add_u32_e32 v1, 0x1b000, v0
	ds_write_b64 v1, v[2:3]
	s_waitcnt vmcnt(8)
	v_cvt_pk_f16_f32 v3, v34, v35
	v_cvt_pk_f16_f32 v2, v32, v33
	v_add_u32_e32 v1, 0x1b800, v0
	ds_write_b64 v1, v[2:3]
	v_add_u32_e32 v1, 0x1c000, v0
	s_waitcnt lgkmcnt(0)
	v_add_u32_e32 v171, 1, v171
	ds_write_b32 v169, v171
	s_waitcnt vmcnt(7)
	v_cvt_pk_f16_f32 v3, v38, v39
	v_cvt_pk_f16_f32 v2, v36, v37
	ds_write_b64 v1, v[2:3]
	s_waitcnt vmcnt(6)
	v_cvt_pk_f16_f32 v3, v42, v43
	v_cvt_pk_f16_f32 v2, v40, v41
	v_add_u32_e32 v1, 0x1c800, v0
	ds_write_b64 v1, v[2:3]
	v_add_u32_e32 v1, 0x1d000, v0
	s_waitcnt vmcnt(5)
	v_cvt_pk_f16_f32 v3, v46, v47
	v_cvt_pk_f16_f32 v2, v44, v45
	ds_write_b64 v1, v[2:3]
	s_waitcnt vmcnt(4)
	v_cvt_pk_f16_f32 v3, v50, v51
	v_cvt_pk_f16_f32 v2, v48, v49
	v_add_u32_e32 v1, 0x1d800, v0
	ds_write_b64 v1, v[2:3]
	v_add_u32_e32 v1, 0x1e000, v0
	s_waitcnt lgkmcnt(0)
	v_add_u32_e32 v171, 1, v171
	ds_write_b32 v169, v171
	s_waitcnt vmcnt(3)
	v_cvt_pk_f16_f32 v3, v54, v55
	v_cvt_pk_f16_f32 v2, v52, v53
	ds_write_b64 v1, v[2:3]
	s_waitcnt vmcnt(2)
	v_cvt_pk_f16_f32 v3, v58, v59
	v_cvt_pk_f16_f32 v2, v56, v57
	v_add_u32_e32 v1, 0x1e800, v0
	ds_write_b64 v1, v[2:3]
	s_waitcnt vmcnt(1)
	v_cvt_pk_f16_f32 v3, v70, v71
	v_cvt_pk_f16_f32 v2, v68, v69
	v_add_u32_e32 v1, 0x1f000, v0
	ds_write_b64 v1, v[2:3]
	s_waitcnt vmcnt(0)
	v_cvt_pk_f16_f32 v3, v74, v75
	v_cvt_pk_f16_f32 v2, v72, v73
	v_add_u32_e32 v0, 0x1f800, v0
	ds_write_b64 v0, v[2:3]
	s_waitcnt lgkmcnt(0)
	v_add_u32_e32 v171, 1, v171
	ds_write_b32 v169, v171
	s_waitcnt lgkmcnt(0)
	s_endpgm
